# layer-0 input conversion loop: next iteration's f32 row loads prefetched into staging registers before the converts and stores
# baseline (speedup 1.0000x reference)
; #define VM_WAIT() asm volatile("s_waitcnt vmcnt(0)" ::: "memory")
; __device__ __forceinline__ void phase_norm1(KArgs args, const float* x, bf16* H, float* rs, int L, LAS unsigned char* lds, int G, int bid, int tid, int wave, int lane) {
;     ...
;         if (x) {
; #pragma unroll 1
;             for (int r0 = 0; r0 < 16; r0 += 2) { f32x4 v[2][4];
; #pragma unroll
;                 for (int r = 0; r < 2; ++r)
; #pragma unroll
;                     for (int j = 0; j < 4; ++j) v[r][j] = __builtin_nontemporal_load((const f32x4*)(x + (size_t)(grp * 16 + r0 + r) * DM) + lane + 64 * j);
; #pragma unroll
;                 for (int r = 0; r < 2; ++r) store_row_bf16(H + (size_t)(grp * 16 + r0 + r) * DM, v[r], 1.f, lane); }
;             VM_WAIT();
.LBB0_34:
	s_and_b64 vcc, exec, s[8:9]
	s_cbranch_vccnz .LBB0_38
	s_ashr_i32 s15, s14, 31
	s_lshl_b64 s[18:19], s[14:15], 12
	s_add_u32 s18, s0, s18
	s_addc_u32 s19, s1, s19
	s_ashr_i32 s17, s16, 31
	s_lshl_b64 s[20:21], s[16:17], 11
	s_add_u32 s20, s10, s20
	s_addc_u32 s21, s11, s21
	s_lshl_b64 s[22:23], s[14:15], 11
	s_add_u32 s22, s10, s22
	s_addc_u32 s23, s11, s23
	s_lshl_b64 s[24:25], s[16:17], 12
	s_add_u32 s24, s0, s24
	s_addc_u32 s25, s1, s25
	s_mov_b32 s15, -2
	v_lshl_add_u64 v[250:251], s[18:19], 0, v[74:75]
	v_lshl_add_u64 v[252:253], s[24:25], 0, v[74:75]
	global_load_dwordx4 v[218:221], v[250:251], off nt
	global_load_dwordx4 v[222:225], v[250:251], off offset:1024 nt
	global_load_dwordx4 v[226:229], v[250:251], off offset:2048 nt
	global_load_dwordx4 v[230:233], v[250:251], off offset:3072 nt
	global_load_dwordx4 v[234:237], v[252:253], off nt
	global_load_dwordx4 v[238:241], v[252:253], off offset:1024 nt
	global_load_dwordx4 v[242:245], v[252:253], off offset:2048 nt
	global_load_dwordx4 v[246:249], v[252:253], off offset:3072 nt
	s_add_u32 s18, s18, 0x2000
	s_addc_u32 s19, s19, 0
	s_add_u32 s24, s24, 0x2000
	s_addc_u32 s25, s25, 0
	s_waitcnt vmcnt(0)
.LBB0_36:
	v_mov_b64_e32 v[2:3], v[218:219]
	v_mov_b64_e32 v[4:5], v[220:221]
	v_mov_b64_e32 v[6:7], v[222:223]
	v_mov_b64_e32 v[8:9], v[224:225]
	v_mov_b64_e32 v[10:11], v[226:227]
	v_mov_b64_e32 v[12:13], v[228:229]
	v_mov_b64_e32 v[14:15], v[230:231]
	v_mov_b64_e32 v[16:17], v[232:233]
	v_mov_b64_e32 v[18:19], v[234:235]
	v_mov_b64_e32 v[20:21], v[236:237]
	v_mov_b64_e32 v[22:23], v[238:239]
	v_mov_b64_e32 v[24:25], v[240:241]
	v_mov_b64_e32 v[26:27], v[242:243]
	v_mov_b64_e32 v[28:29], v[244:245]
	v_mov_b64_e32 v[30:31], v[246:247]
	v_mov_b64_e32 v[32:33], v[248:249]
	s_add_i32 s15, s15, 2
	v_lshl_add_u64 v[36:37], s[20:21], 0, v[76:77]
	s_add_u32 s20, s20, 0x1000
	s_addc_u32 s21, s21, 0
	v_lshl_add_u64 v[34:35], s[22:23], 0, v[76:77]
	s_add_u32 s22, s22, 0x1000
	s_addc_u32 s23, s23, 0
	v_lshl_add_u64 v[250:251], s[18:19], 0, v[74:75]
	v_lshl_add_u64 v[252:253], s[24:25], 0, v[74:75]
	s_add_u32 s18, s18, 0x2000
	s_addc_u32 s19, s19, 0
	s_add_u32 s24, s24, 0x2000
	s_addc_u32 s25, s25, 0
	s_cmp_gt_u32 s15, 13
	s_cbranch_scc1 .Lx_noload
	global_load_dwordx4 v[218:221], v[250:251], off nt
	global_load_dwordx4 v[222:225], v[250:251], off offset:1024 nt
	global_load_dwordx4 v[226:229], v[250:251], off offset:2048 nt
	global_load_dwordx4 v[230:233], v[250:251], off offset:3072 nt
	global_load_dwordx4 v[234:237], v[252:253], off nt
	global_load_dwordx4 v[238:241], v[252:253], off offset:1024 nt
	global_load_dwordx4 v[242:245], v[252:253], off offset:2048 nt
	global_load_dwordx4 v[246:249], v[252:253], off offset:3072 nt
.Lx_noload:
	v_cvt_pk_bf16_f32 v2, v2, v3
	v_cvt_pk_bf16_f32 v3, v4, v5
	v_cvt_pk_bf16_f32 v4, v6, v7
	v_cvt_pk_bf16_f32 v5, v8, v9
	v_cvt_pk_bf16_f32 v6, v10, v11
	v_cvt_pk_bf16_f32 v7, v12, v13
	v_cvt_pk_bf16_f32 v8, v14, v15
	v_cvt_pk_bf16_f32 v9, v16, v17
	v_cvt_pk_bf16_f32 v10, v18, v19
	v_cvt_pk_bf16_f32 v11, v20, v21
	v_cvt_pk_bf16_f32 v12, v22, v23
	v_cvt_pk_bf16_f32 v13, v24, v25
	v_cvt_pk_bf16_f32 v14, v26, v27
	v_cvt_pk_bf16_f32 v15, v28, v29
	v_cvt_pk_bf16_f32 v16, v30, v31
	v_cvt_pk_bf16_f32 v17, v32, v33
	global_store_dwordx2 v[34:35], v[2:3], off
	global_store_dwordx2 v[34:35], v[4:5], off offset:512
	global_store_dwordx2 v[34:35], v[6:7], off offset:1024
	global_store_dwordx2 v[34:35], v[8:9], off offset:1536
	global_store_dwordx2 v[36:37], v[10:11], off
	global_store_dwordx2 v[36:37], v[12:13], off offset:512
	global_store_dwordx2 v[36:37], v[14:15], off offset:1024
	global_store_dwordx2 v[36:37], v[16:17], off offset:1536
	s_waitcnt vmcnt(8)
	s_cbranch_scc0 .LBB0_36
	s_waitcnt vmcnt(0)
